# attention softmax: shortened wave-uniform lazy-rescale test (fast path: one compare + s_cmp + branch, alpha = 1 and m kept when every lane is within the threshold; the long form only on the rare path)
# speedup vs baseline: 1.0014x; 1.0014x over previous
; DEV void partialSM(f32x16& p0, f32x16& p1, float& m_reg, float& mn, float& alpha) {
;   constexpr float C = SCALE * 1.4426950408889634f;
;   float pmax = p0[0];
; #pragma unroll
;   for (int r = 1; r < 16; ++r) pmax = fmaxf(pmax, p0[r]);
; #pragma unroll
;   for (int r = 0; r < 16; ++r) pmax = fmaxf(pmax, p1[r]);
;   { auto rr = __builtin_amdgcn_permlane32_swap(__float_as_uint(pmax), __float_as_uint(pmax), false, false);
;     pmax = fmaxf(__uint_as_float(rr[0]), __uint_as_float(rr[1])); }
;   if (__builtin_expect(__all(pmax - m_reg <= THR / SCALE), 1)) { mn = m_reg; alpha = 1.f; }
;   else { mn = fmaxf(m_reg, pmax); alpha = __builtin_amdgcn_exp2f((m_reg - mn) * C); m_reg = mn; }
; DEV void qkt(f32x16& p0, f32x16& p1, const char* Ks, const bf16x8* qr, int r32, int hi) {
;   p0 = f32x16{}; p1 = f32x16{};
;   __builtin_amdgcn_s_setprio(1);
; #pragma unroll
;   for (int d0 = 0; d0 < 12; ++d0) { const int cb = (d0 * 16 + hi * 8) * 2;
;     const bf16x8 b0 = *reinterpret_cast<const bf16x8*>(Ks + KSWZ2(r32, cb));
;     const bf16x8 b1 = *reinterpret_cast<const bf16x8*>(Ks + KSWZ2(32 + r32, cb));
;     p0 = __builtin_amdgcn_mfma_f32_32x32x16_bf16(b0, qr[d0], p0, 0, 0, 0);
;     p1 = __builtin_amdgcn_mfma_f32_32x32x16_bf16(b1, qr[d0], p1, 0, 0, 0); }
;   __builtin_amdgcn_s_setprio(0);
; }
.Lfst_a_end:
.LBB0_907:
	s_lshl_b32 s6, s36, 15
	s_add_i32 s6, s6, 0
	s_setprio 1
	v_add3_u32 v66, s6, v201, v200
	ds_read_b128 v[68:71], v66 offset:32768
	ds_read_b128 v[72:75], v66 offset:49152
	v_add3_u32 v66, s6, v202, v200
	ds_read_b128 v[224:227], v66 offset:32768
	ds_read_b128 v[228:231], v66 offset:49152
	v_add3_u32 v66, s6, v203, v200
	s_waitcnt lgkmcnt(0)
	v_mfma_f32_32x32x16_bf16 v[84:99], v[68:71], v[100:103], 0
	v_mfma_f32_32x32x16_bf16 v[68:83], v[72:75], v[100:103], 0
	v_mfma_f32_32x32x16_bf16 v[84:99], v[224:227], v[104:107], v[84:99]
	v_mfma_f32_32x32x16_bf16 v[68:83], v[228:231], v[104:107], v[68:83]
	ds_read_b128 v[224:227], v66 offset:32768
	ds_read_b128 v[228:231], v66 offset:49152
	v_add3_u32 v66, s6, v204, v200
	s_waitcnt lgkmcnt(1)
	v_mfma_f32_32x32x16_bf16 v[84:99], v[224:227], v[108:111], v[84:99]
	s_waitcnt lgkmcnt(0)
	v_mfma_f32_32x32x16_bf16 v[68:83], v[228:231], v[108:111], v[68:83]
	ds_read_b128 v[224:227], v66 offset:32768
	ds_read_b128 v[228:231], v66 offset:49152
	v_add3_u32 v66, s6, v205, v200
	s_waitcnt lgkmcnt(1)
	v_mfma_f32_32x32x16_bf16 v[84:99], v[224:227], v[112:115], v[84:99]
	s_waitcnt lgkmcnt(0)
	v_mfma_f32_32x32x16_bf16 v[68:83], v[228:231], v[112:115], v[68:83]
	ds_read_b128 v[224:227], v66 offset:32768
	ds_read_b128 v[228:231], v66 offset:49152
	v_add3_u32 v66, s6, v206, v200
	s_waitcnt lgkmcnt(1)
	v_mfma_f32_32x32x16_bf16 v[84:99], v[224:227], v[116:119], v[84:99]
	s_waitcnt lgkmcnt(0)
	v_mfma_f32_32x32x16_bf16 v[68:83], v[228:231], v[116:119], v[68:83]
	ds_read_b128 v[224:227], v66 offset:32768
	ds_read_b128 v[228:231], v66 offset:49152
	v_add3_u32 v66, s6, v207, v200
	s_waitcnt lgkmcnt(1)
	v_mfma_f32_32x32x16_bf16 v[84:99], v[224:227], v[120:123], v[84:99]
	s_waitcnt lgkmcnt(0)
	v_mfma_f32_32x32x16_bf16 v[68:83], v[228:231], v[120:123], v[68:83]
	ds_read_b128 v[224:227], v66 offset:32768
	ds_read_b128 v[228:231], v66 offset:49152
	v_add3_u32 v66, s6, v208, v200
	s_waitcnt lgkmcnt(1)
	v_mfma_f32_32x32x16_bf16 v[84:99], v[224:227], v[124:127], v[84:99]
	s_waitcnt lgkmcnt(0)
	v_mfma_f32_32x32x16_bf16 v[68:83], v[228:231], v[124:127], v[68:83]
	ds_read_b128 v[224:227], v66 offset:32768
	ds_read_b128 v[228:231], v66 offset:49152
	v_add3_u32 v66, s6, v209, v200
	s_waitcnt lgkmcnt(1)
	v_mfma_f32_32x32x16_bf16 v[84:99], v[224:227], v[128:131], v[84:99]
	s_waitcnt lgkmcnt(0)
	v_mfma_f32_32x32x16_bf16 v[68:83], v[228:231], v[128:131], v[68:83]
	ds_read_b128 v[224:227], v66 offset:32768
	ds_read_b128 v[228:231], v66 offset:49152
	v_add3_u32 v66, s6, v211, v200
	s_waitcnt lgkmcnt(1)
	v_mfma_f32_32x32x16_bf16 v[84:99], v[224:227], v[132:135], v[84:99]
	s_waitcnt lgkmcnt(0)
	v_mfma_f32_32x32x16_bf16 v[68:83], v[228:231], v[132:135], v[68:83]
	ds_read_b128 v[224:227], v66 offset:32768
	ds_read_b128 v[228:231], v66 offset:49152
	v_add3_u32 v66, s6, v212, v200
	s_waitcnt lgkmcnt(1)
	v_mfma_f32_32x32x16_bf16 v[84:99], v[224:227], v[140:143], v[84:99]
	s_waitcnt lgkmcnt(0)
	v_mfma_f32_32x32x16_bf16 v[68:83], v[228:231], v[140:143], v[68:83]
	ds_read_b128 v[224:227], v66 offset:32768
	ds_read_b128 v[228:231], v66 offset:49152
	v_add3_u32 v66, s6, v213, v200
	s_waitcnt lgkmcnt(1)
	v_mfma_f32_32x32x16_bf16 v[84:99], v[224:227], v[136:139], v[84:99]
	s_waitcnt lgkmcnt(0)
	v_mfma_f32_32x32x16_bf16 v[68:83], v[228:231], v[136:139], v[68:83]
	ds_read_b128 v[224:227], v66 offset:32768
	ds_read_b128 v[228:231], v66 offset:49152
	s_waitcnt lgkmcnt(1)
	v_mfma_f32_32x32x16_bf16 v[84:99], v[224:227], v[144:147], v[84:99]
	s_waitcnt lgkmcnt(0)
	v_mfma_f32_32x32x16_bf16 v[68:83], v[228:231], v[144:147], v[68:83]
	s_setprio 0
	s_nop 8
	v_max_f32_e32 v66, v85, v85
	v_max_f32_e32 v219, v84, v84
	v_max_f32_e32 v66, v219, v66
	v_max3_f32 v66, v66, v86, v87
	v_max3_f32 v66, v66, v88, v89
	v_max3_f32 v66, v66, v90, v91
	v_max3_f32 v66, v66, v92, v93
	v_max3_f32 v66, v66, v94, v95
	v_max3_f32 v66, v66, v96, v97
	v_max3_f32 v66, v66, v98, v99
	v_max3_f32 v66, v66, v68, v69
	v_max3_f32 v66, v66, v70, v71
	v_max3_f32 v66, v66, v72, v73
	v_max3_f32 v66, v66, v74, v75
	v_max3_f32 v66, v66, v76, v77
	v_max3_f32 v66, v66, v78, v79
	v_max3_f32 v66, v66, v80, v81
	v_max3_f32 v66, v66, v82, v83
	v_mov_b32_e32 v219, v66
	s_nop 1
	v_permlane32_swap_b32_e32 v66, v219
	v_max_f32_e32 v219, v219, v219
	v_max_f32_e32 v66, v66, v66
	v_max_f32_e32 v66, v66, v219
	v_sub_f32_e32 v219, v66, v215
	v_cmp_ge_f32_e32 vcc, s31, v219
	s_cmp_eq_u64 vcc, exec
	s_cbranch_scc0 .Lresc_a
	v_mov_b32_e32 v219, 1.0
	s_branch .Lnor_a
.Lresc_a:
	v_max_f32_e32 v220, v215, v215
	v_sub_f32_e32 v219, v66, v215
	v_max_f32_e32 v66, v220, v66
	v_sub_f32_e32 v220, v215, v66
	v_mul_f32_e32 v220, 0x3dd53b94, v220
	v_exp_f32_e32 v220, v220
	v_cmp_ge_f32_e32 vcc, s31, v219
	s_cmp_eq_u64 vcc, exec
	s_cselect_b64 s[6:7], -1, 0
	v_cndmask_b32_e64 v219, v220, 1.0, s[6:7]
	v_cmp_gt_f32_e32 vcc, 1.0, v219
	s_cbranch_vccz .LBB0_911
	s_and_saveexec_b64 s[24:25], s[4:5]
	ds_write_b32 v210, v219 offset:128
	s_or_b64 exec, exec, s[24:25]
	s_waitcnt lgkmcnt(0)
	v_add_u32_e32 v220, v185, v186
	ds_read_b128 v[224:227], v220 offset:224
	ds_read_b128 v[228:231], v220 offset:192
	ds_read_b128 v[232:235], v220 offset:160
	ds_read_b128 v[236:239], v220 offset:128
	s_waitcnt lgkmcnt(3)
	v_pk_mul_f32 v[62:63], v[62:63], v[224:225]
	s_waitcnt lgkmcnt(2)
	v_pk_mul_f32 v[58:59], v[58:59], v[228:229]
	s_waitcnt lgkmcnt(1)
	v_pk_mul_f32 v[54:55], v[54:55], v[232:233]
	v_pk_mul_f32 v[64:65], v[64:65], v[226:227]
	v_pk_mul_f32 v[60:61], v[60:61], v[230:231]
	v_pk_mul_f32 v[56:57], v[56:57], v[234:235]
	s_waitcnt lgkmcnt(0)
	v_pk_mul_f32 v[52:53], v[52:53], v[238:239]
	v_pk_mul_f32 v[50:51], v[50:51], v[236:237]
	v_pk_mul_f32 v[46:47], v[46:47], v[224:225]
	v_pk_mul_f32 v[42:43], v[42:43], v[228:229]
	v_pk_mul_f32 v[38:39], v[38:39], v[232:233]
	v_pk_mul_f32 v[48:49], v[48:49], v[226:227]
	v_pk_mul_f32 v[44:45], v[44:45], v[230:231]
	v_pk_mul_f32 v[40:41], v[40:41], v[234:235]
	v_pk_mul_f32 v[36:37], v[36:37], v[238:239]
	v_pk_mul_f32 v[34:35], v[34:35], v[236:237]
	v_pk_mul_f32 v[30:31], v[30:31], v[224:225]
	v_pk_mul_f32 v[26:27], v[26:27], v[228:229]
	v_pk_mul_f32 v[22:23], v[22:23], v[232:233]
	v_pk_mul_f32 v[32:33], v[32:33], v[226:227]
	v_pk_mul_f32 v[28:29], v[28:29], v[230:231]
	v_pk_mul_f32 v[24:25], v[24:25], v[234:235]
	v_pk_mul_f32 v[20:21], v[20:21], v[238:239]
	v_pk_mul_f32 v[18:19], v[18:19], v[236:237]
	v_pk_mul_f32 v[14:15], v[14:15], v[224:225]
	v_pk_mul_f32 v[10:11], v[10:11], v[228:229]
	v_pk_mul_f32 v[6:7], v[6:7], v[232:233]
	v_pk_mul_f32 v[16:17], v[16:17], v[226:227]
	v_pk_mul_f32 v[12:13], v[12:13], v[230:231]
	v_pk_mul_f32 v[8:9], v[8:9], v[234:235]
	v_pk_mul_f32 v[4:5], v[4:5], v[238:239]
	v_pk_mul_f32 v[2:3], v[2:3], v[236:237]

; #define SBAR() __builtin_amdgcn_sched_barrier(0)
; #define PV_WAIT(n) do { asm volatile("s_waitcnt lgkmcnt(" #n ")" ::: "memory"); SBAR(); } while (0)
; DEV void partialSM(f32x16& p0, f32x16& p1, float& m_reg, float& mn, float& alpha) {
;     ...
;   const float mnC = -mn * C;
; #pragma unroll
;   for (int r = 0; r < 16; ++r) p0[r] = fmaf(p0[r], C, mnC);
; #pragma unroll
;   for (int r = 0; r < 16; ++r) p1[r] = fmaf(p1[r], C, mnC);
; #pragma unroll
;   for (int r = 0; r < 16; ++r) p0[r] = __builtin_amdgcn_exp2f(p0[r]);
; }
; DEV void finishSM(f32x16& p0, f32x16& p1, float alpha, float& l_reg, bf16x8& pa0, bf16x8& pa1, bf16x8& pa2, bf16x8& pa3) {
; #pragma unroll
;   for (int r = 0; r < 16; ++r) p1[r] = __builtin_amdgcn_exp2f(p1[r]);
;   float ps = 0;
; #pragma unroll
;   for (int r = 0; r < 16; ++r) ps += p0[r];
; #pragma unroll
;   for (int r = 0; r < 16; ++r) ps += p1[r];
;   { auto rr = __builtin_amdgcn_permlane32_swap(__float_as_uint(ps), __float_as_uint(ps), false, false);
;     ps = __uint_as_float(rr[0]) + __uint_as_float(rr[1]); }
;   l_reg = l_reg * alpha + ps;
;     ...
;   PK4(p0, 0, pa0); PK4(p0, 8, pa1); PK4(p1, 0, pa2); PK4(p1, 8, pa3);
;     ...
; }
; DEV void pv_mma(f32x16& od, const VFrag& f, bf16x8 pa0, bf16x8 pa1, bf16x8 pa2, bf16x8 pa3) {
;     ...
;   __builtin_amdgcn_s_setprio(1);
;   od = __builtin_amdgcn_mfma_f32_32x32x16_bf16(pa0, PK(f.l0, f.h0), od, 0, 0, 0);
;   od = __builtin_amdgcn_mfma_f32_32x32x16_bf16(pa1, PK(f.l1, f.h1), od, 0, 0, 0);
;   od = __builtin_amdgcn_mfma_f32_32x32x16_bf16(pa2, PK(f.l2, f.h2), od, 0, 0, 0);
;   od = __builtin_amdgcn_mfma_f32_32x32x16_bf16(pa3, PK(f.l3, f.h3), od, 0, 0, 0);
;   __builtin_amdgcn_s_setprio(0);
;     ...
; }
; DEV void pv_d0(f32x16* o, int vb, bf16x8 pa0, bf16x8 pa1, bf16x8 pa2, bf16x8 pa3) {
;   VFrag fa, fb;
;   pv_read<0>(fa, vb);
;   pv_read<1>(fb, vb); PV_WAIT(8); pv_mma(o[0], fa, pa0, pa1, pa2, pa3); SBAR();
;   pv_read<2>(fa, vb); PV_WAIT(8); pv_mma(o[1], fb, pa0, pa1, pa2, pa3); SBAR();
;   pv_read<3>(fb, vb); PV_WAIT(8); pv_mma(o[2], fa, pa0, pa1, pa2, pa3); SBAR();
;   PV_WAIT(0); pv_mma(o[3], fb, pa0, pa1, pa2, pa3);
.Lnor_a:
	v_mul_f32_e32 v66, 0xbdd53b94, v215
	v_fmamk_f32 v84, v84, 0x3dd53b94, v66
	v_fmamk_f32 v85, v85, 0x3dd53b94, v66
	v_fmamk_f32 v86, v86, 0x3dd53b94, v66
	v_fmamk_f32 v87, v87, 0x3dd53b94, v66
	v_fmamk_f32 v88, v88, 0x3dd53b94, v66
	v_fmamk_f32 v89, v89, 0x3dd53b94, v66
	v_fmamk_f32 v90, v90, 0x3dd53b94, v66
	v_fmamk_f32 v91, v91, 0x3dd53b94, v66
	v_fmamk_f32 v92, v92, 0x3dd53b94, v66
	v_fmamk_f32 v93, v93, 0x3dd53b94, v66
	v_fmamk_f32 v94, v94, 0x3dd53b94, v66
	v_fmamk_f32 v95, v95, 0x3dd53b94, v66
	v_fmamk_f32 v96, v96, 0x3dd53b94, v66
	v_fmamk_f32 v97, v97, 0x3dd53b94, v66
	v_fmamk_f32 v98, v98, 0x3dd53b94, v66
	v_fmamk_f32 v99, v99, 0x3dd53b94, v66
	v_fmamk_f32 v68, v68, 0x3dd53b94, v66
	v_fmamk_f32 v69, v69, 0x3dd53b94, v66
	v_fmamk_f32 v70, v70, 0x3dd53b94, v66
	v_fmamk_f32 v71, v71, 0x3dd53b94, v66
	v_fmamk_f32 v72, v72, 0x3dd53b94, v66
	v_fmamk_f32 v73, v73, 0x3dd53b94, v66
	v_fmamk_f32 v74, v74, 0x3dd53b94, v66
	v_fmamk_f32 v75, v75, 0x3dd53b94, v66
	v_fmamk_f32 v76, v76, 0x3dd53b94, v66
	v_fmamk_f32 v77, v77, 0x3dd53b94, v66
	v_fmamk_f32 v78, v78, 0x3dd53b94, v66
	v_fmamk_f32 v79, v79, 0x3dd53b94, v66
	v_fmamk_f32 v80, v80, 0x3dd53b94, v66
	v_fmamk_f32 v81, v81, 0x3dd53b94, v66
	v_fmamk_f32 v82, v82, 0x3dd53b94, v66
	v_fmac_f32_e32 v66, 0x3dd53b94, v83
	v_exp_f32_e32 v83, v84
	v_exp_f32_e32 v84, v85
	v_exp_f32_e32 v85, v86
	v_exp_f32_e32 v86, v87
	v_exp_f32_e32 v87, v88
	v_exp_f32_e32 v88, v89
	v_exp_f32_e32 v89, v90
	v_exp_f32_e32 v90, v91
	v_exp_f32_e32 v91, v92
	v_exp_f32_e32 v92, v93
	v_exp_f32_e32 v93, v94
	v_exp_f32_e32 v94, v95
	v_exp_f32_e32 v95, v96
	v_exp_f32_e32 v96, v97
	v_exp_f32_e32 v97, v98
	v_exp_f32_e32 v98, v99
	v_exp_f32_e32 v99, v68
	v_add_f32_e32 v68, 0, v83
	v_add_f32_e32 v68, v84, v68
	v_add_f32_e32 v68, v85, v68
	v_add_f32_e32 v68, v86, v68
	v_add_f32_e32 v68, v87, v68
	v_add_f32_e32 v68, v88, v68
	v_add_f32_e32 v68, v89, v68
	v_add_f32_e32 v68, v90, v68
	v_add_f32_e32 v68, v91, v68
	v_add_f32_e32 v68, v92, v68
	v_add_f32_e32 v68, v93, v68
	v_add_f32_e32 v68, v94, v68
	v_add_f32_e32 v68, v95, v68
	v_exp_f32_e32 v220, v69
	v_add_f32_e32 v68, v96, v68
	v_exp_f32_e32 v221, v70
	v_add_f32_e32 v68, v97, v68
	v_exp_f32_e32 v222, v71
	v_add_f32_e32 v68, v98, v68
	v_exp_f32_e32 v224, v72
	v_add_f32_e32 v68, v99, v68
	v_exp_f32_e32 v225, v73
	v_add_f32_e32 v68, v220, v68
	v_exp_f32_e32 v226, v74
	v_add_f32_e32 v68, v221, v68
	v_exp_f32_e32 v227, v75
	v_add_f32_e32 v68, v222, v68
	v_exp_f32_e32 v228, v76
	v_add_f32_e32 v68, v224, v68
	v_exp_f32_e32 v229, v77
	v_add_f32_e32 v68, v225, v68
	v_exp_f32_e32 v230, v78
	v_add_f32_e32 v68, v226, v68
	v_exp_f32_e32 v231, v79
	v_add_f32_e32 v68, v227, v68
	v_exp_f32_e32 v232, v80
	v_add_f32_e32 v68, v228, v68
	v_exp_f32_e32 v233, v81
	v_add_f32_e32 v68, v229, v68
	v_exp_f32_e32 v234, v82
	v_add_f32_e32 v68, v230, v68
	v_exp_f32_e32 v66, v66
	v_add_f32_e32 v68, v231, v68
	v_add_f32_e32 v68, v232, v68
	v_add_f32_e32 v68, v233, v68
	v_add_f32_e32 v68, v234, v68
	v_add_f32_e32 v68, v66, v68
	v_mov_b32_e32 v69, v68
	s_nop 1
	v_permlane32_swap_b32_e32 v68, v69
	v_cvt_pk_bf16_f32 v70, v83, v84
	v_cvt_pk_bf16_f32 v71, v85, v86
	v_cvt_pk_bf16_f32 v72, v87, v88
	v_cvt_pk_bf16_f32 v73, v89, v90
	v_cvt_pk_bf16_f32 v74, v91, v92
	v_cvt_pk_bf16_f32 v75, v93, v94
	v_cvt_pk_bf16_f32 v76, v95, v96
	v_cvt_pk_bf16_f32 v77, v97, v98
	v_cvt_pk_bf16_f32 v78, v99, v220
	v_cvt_pk_bf16_f32 v79, v221, v222
	v_cvt_pk_bf16_f32 v80, v224, v225
	v_cvt_pk_bf16_f32 v81, v226, v227
	v_cvt_pk_bf16_f32 v82, v228, v229
	v_cvt_pk_bf16_f32 v83, v230, v231
	v_cvt_pk_bf16_f32 v84, v232, v233
	v_cvt_pk_bf16_f32 v85, v234, v66
	v_permlane32_swap_b32_e32 v70, v72
	v_permlane32_swap_b32_e32 v71, v73
	v_permlane32_swap_b32_e32 v74, v76
	v_permlane32_swap_b32_e32 v75, v77
	v_permlane32_swap_b32_e32 v78, v80
	v_permlane32_swap_b32_e32 v79, v81
	v_permlane32_swap_b32_e32 v82, v84
	v_permlane32_swap_b32_e32 v83, v85
	v_lshl_add_u32 v66, s36, 14, v214
	ds_read_b64_tr_b16 v[86:87], v66 offset:0
	ds_read_b64_tr_b16 v[88:89], v66 offset:0x800
	ds_read_b64_tr_b16 v[90:91], v66 offset:0x1000
	ds_read_b64_tr_b16 v[92:93], v66 offset:0x1800
	ds_read_b64_tr_b16 v[94:95], v66 offset:0x2000
	ds_read_b64_tr_b16 v[96:97], v66 offset:0x2800
	ds_read_b64_tr_b16 v[224:225], v66 offset:0x3000
	ds_read_b64_tr_b16 v[226:227], v66 offset:0x3800
	ds_read_b64_tr_b16 v[228:229], v66 offset:0x200
	ds_read_b64_tr_b16 v[230:231], v66 offset:0xa00
	ds_read_b64_tr_b16 v[232:233], v66 offset:0x1200
	ds_read_b64_tr_b16 v[234:235], v66 offset:0x1a00
	ds_read_b64_tr_b16 v[236:237], v66 offset:0x2200
	ds_read_b64_tr_b16 v[238:239], v66 offset:0x2a00
	ds_read_b64_tr_b16 v[240:241], v66 offset:0x3200
	ds_read_b64_tr_b16 v[242:243], v66 offset:0x3a00
	s_waitcnt lgkmcnt(8)
	s_setprio 1
	v_mfma_f32_32x32x16_bf16 v[50:65], v[70:73], v[86:89], v[50:65]
	v_mfma_f32_32x32x16_bf16 v[50:65], v[74:77], v[90:93], v[50:65]
	v_mfma_f32_32x32x16_bf16 v[50:65], v[78:81], v[94:97], v[50:65]
	v_mfma_f32_32x32x16_bf16 v[50:65], v[82:85], v[224:227], v[50:65]
	s_setprio 0
	ds_read_b64_tr_b16 v[86:87], v66 offset:0x400
	ds_read_b64_tr_b16 v[88:89], v66 offset:0xc00
	ds_read_b64_tr_b16 v[90:91], v66 offset:0x1400
	ds_read_b64_tr_b16 v[92:93], v66 offset:0x1c00
	ds_read_b64_tr_b16 v[94:95], v66 offset:0x2400
	ds_read_b64_tr_b16 v[96:97], v66 offset:0x2c00
	ds_read_b64_tr_b16 v[224:225], v66 offset:0x3400
	ds_read_b64_tr_b16 v[226:227], v66 offset:0x3c00
	s_waitcnt lgkmcnt(8)
	s_setprio 1
	v_mfma_f32_32x32x16_bf16 v[34:49], v[70:73], v[228:231], v[34:49]
	v_mfma_f32_32x32x16_bf16 v[34:49], v[74:77], v[232:235], v[34:49]
	v_mfma_f32_32x32x16_bf16 v[34:49], v[78:81], v[236:239], v[34:49]
	v_mfma_f32_32x32x16_bf16 v[34:49], v[82:85], v[240:243], v[34:49]
	s_setprio 0
	ds_read_b64_tr_b16 v[228:229], v66 offset:0x600
	ds_read_b64_tr_b16 v[230:231], v66 offset:0xe00
	ds_read_b64_tr_b16 v[232:233], v66 offset:0x1600
	ds_read_b64_tr_b16 v[234:235], v66 offset:0x1e00
	ds_read_b64_tr_b16 v[236:237], v66 offset:0x2600
	ds_read_b64_tr_b16 v[238:239], v66 offset:0x2e00
	ds_read_b64_tr_b16 v[240:241], v66 offset:0x3600
	ds_read_b64_tr_b16 v[242:243], v66 offset:0x3e00
	s_waitcnt lgkmcnt(8)
	s_setprio 1
	v_mfma_f32_32x32x16_bf16 v[18:33], v[70:73], v[86:89], v[18:33]
	v_mfma_f32_32x32x16_bf16 v[18:33], v[74:77], v[90:93], v[18:33]
	v_mfma_f32_32x32x16_bf16 v[18:33], v[78:81], v[94:97], v[18:33]
	v_mfma_f32_32x32x16_bf16 v[18:33], v[82:85], v[224:227], v[18:33]
	s_setprio 0
	s_waitcnt lgkmcnt(0)
	s_setprio 1
	v_mfma_f32_32x32x16_bf16 v[2:17], v[70:73], v[228:231], v[2:17]
	v_mfma_f32_32x32x16_bf16 v[2:17], v[74:77], v[232:235], v[2:17]
	v_mfma_f32_32x32x16_bf16 v[2:17], v[78:81], v[236:239], v[2:17]
	v_mfma_f32_32x32x16_bf16 v[2:17], v[82:85], v[240:243], v[2:17]
	s_setprio 0
	s_cmp_gt_u32 s37, 62
	s_cbranch_scc1 .LBB0_919
; DEV int ltid() { int t = threadIdx.x; asm volatile("" : "+v"(t)); return t; }
; DEV unsigned cvt_pk4_fp8(f32x4 v) { unsigned r = 0; r = __builtin_amdgcn_cvt_pk_fp8_f32(v[0], v[1], r, false); r = __builtin_amdgcn_cvt_pk_fp8_f32(v[2], v[3], r, true); return r; }
; DEV void fill_load(CParams& p, int wg, int slot, f32x4 (&ld)[4]) {
;   const FillDesc d = fill_decode(p, wg, slot); const int tid = ltid(), tx = tid & 15, ty = tid >> 4;
;   const float* sp = d.src + (long)(d.kh + 4 * ty) * d.ldsrc + d.n0 + 4 * tx;
; #pragma unroll
;   for (int r = 0; r < 4; ++r) ld[r] = *(const f32x4*)(sp + (long)r * d.ldsrc);
; }
; DEV void fill_write(const f32x4 (&ld)[4], int bufsel) {
;   extern __shared__ __attribute__((aligned(16))) char shm[];
;   unsigned* T = (unsigned*)(shm + FILL_LDS_OFF + bufsel * FILL_TB); const int tid = ltid(), tx = tid & 15, ty = tid >> 4;
;   constexpr float WS = (float)(1 << FP8_WSCALE_LOG2_);
; #pragma unroll
;   for (int j = 0; j < 4; ++j) T[(4 * tx + j) * 33 + ty] = cvt_pk4_fp8((f32x4){ld[0][j] * WS, ld[1][j] * WS, ld[2][j] * WS, ld[3][j] * WS});
; }
; DEV void attn_unit(const bf16_t* __restrict__ Qb, const bf16_t* __restrict__ Kh, const bf16_t* __restrict__ Vh, const float* __restrict__ rp, bf16_t* __restrict__ Ob, CParams& fp, int fwg, int fbase, int fn) {
;     ...
;     if (j < fn) { fill_write(fld, j & 1); if (j + 1 < fn) fill_load(fp, fwg, fbase + j + 1, fld); }
	s_waitcnt vmcnt(3)
	v_mul_f32_e32 v71, 0x42800000, v168
	s_waitcnt vmcnt(2)
	v_mul_f32_e32 v72, 0x42800000, v172
	v_cvt_pk_fp8_f32 v73, v71, v72
	s_waitcnt vmcnt(1)
	v_mul_f32_e32 v71, 0x42800000, v176
	s_waitcnt vmcnt(0)
	v_mul_f32_e32 v72, 0x42800000, v180
	v_cvt_pk_fp8_f32 v73, v71, v72 op_sel:[0,0,1]
	v_mul_f32_e32 v71, 0x42800000, v169
	v_mul_f32_e32 v72, 0x42800000, v173
	v_cvt_pk_fp8_f32 v74, v71, v72
	v_mul_f32_e32 v71, 0x42800000, v177
	v_mul_f32_e32 v72, 0x42800000, v181
	v_cvt_pk_fp8_f32 v74, v71, v72 op_sel:[0,0,1]
	v_mul_f32_e32 v71, 0x42800000, v170
	v_mul_f32_e32 v72, 0x42800000, v174
	v_cvt_pk_fp8_f32 v77, v71, v72
	v_mul_f32_e32 v71, 0x42800000, v171
	v_mul_f32_e32 v72, 0x42800000, v175
	v_cvt_pk_fp8_f32 v78, v71, v72
	v_mul_f32_e32 v75, 0x42800000, v178
	v_mul_f32_e32 v76, 0x42800000, v182
	v_mul_f32_e32 v71, 0x42800000, v179
	v_mul_f32_e32 v72, 0x42800000, v183
	v_cvt_pk_fp8_f32 v77, v75, v76 op_sel:[0,0,1]
	v_cvt_pk_fp8_f32 v78, v71, v72 op_sel:[0,0,1]
	s_mul_i32 s56, s36, 0x2200
	s_cmp_eq_u32 s34, 60
	v_add_u32_e32 v66, s56, v245
	ds_write2_b32 v66, v73, v74 offset1:33
	ds_write2_b32 v66, v77, v78 offset0:66 offset1:99
	s_cbranch_scc1 .LBB0_919
	s_cmp_lg_u32 s37, 60
	s_cbranch_scc1 .Lfld_a
	s_mov_b64 s[62:63], s[20:21]
	v_mov_b32_e32 v248, v252
	v_add_u32_e32 v249, 0x2000, v252
	v_add_u32_e32 v250, 0x4000, v252
	v_add_u32_e32 v251, 0x6000, v252

; DEV void partialSM(f32x16& p0, f32x16& p1, float& m_reg, float& mn, float& alpha) {
;   constexpr float C = SCALE * 1.4426950408889634f;
;   float pmax = p0[0];
; #pragma unroll
;   for (int r = 1; r < 16; ++r) pmax = fmaxf(pmax, p0[r]);
; #pragma unroll
;   for (int r = 0; r < 16; ++r) pmax = fmaxf(pmax, p1[r]);
;   { auto rr = __builtin_amdgcn_permlane32_swap(__float_as_uint(pmax), __float_as_uint(pmax), false, false);
;     pmax = fmaxf(__uint_as_float(rr[0]), __uint_as_float(rr[1])); }
;   if (__builtin_expect(__all(pmax - m_reg <= THR / SCALE), 1)) { mn = m_reg; alpha = 1.f; }
;   else { mn = fmaxf(m_reg, pmax); alpha = __builtin_amdgcn_exp2f((m_reg - mn) * C); m_reg = mn; }
; DEV void qkt(f32x16& p0, f32x16& p1, const char* Ks, const bf16x8* qr, int r32, int hi) {
;   p0 = f32x16{}; p1 = f32x16{};
;   __builtin_amdgcn_s_setprio(1);
; #pragma unroll
;   for (int d0 = 0; d0 < 12; ++d0) { const int cb = (d0 * 16 + hi * 8) * 2;
;     const bf16x8 b0 = *reinterpret_cast<const bf16x8*>(Ks + KSWZ2(r32, cb));
;     const bf16x8 b1 = *reinterpret_cast<const bf16x8*>(Ks + KSWZ2(32 + r32, cb));
;     p0 = __builtin_amdgcn_mfma_f32_32x32x16_bf16(b0, qr[d0], p0, 0, 0, 0);
;     p1 = __builtin_amdgcn_mfma_f32_32x32x16_bf16(b1, qr[d0], p1, 0, 0, 0); }
;   __builtin_amdgcn_s_setprio(0);
; }
.LBB0_1114:
	s_lshl_b32 s6, s37, 15
	s_add_i32 s6, s6, 0
	s_setprio 1
	v_add3_u32 v66, s6, v201, v200
	ds_read_b128 v[68:71], v66 offset:32768
	ds_read_b128 v[72:75], v66 offset:49152
	v_add3_u32 v66, s6, v202, v200
	ds_read_b128 v[224:227], v66 offset:32768
	ds_read_b128 v[228:231], v66 offset:49152
	v_add3_u32 v66, s6, v203, v200
	s_waitcnt lgkmcnt(0)
	v_mfma_f32_32x32x16_bf16 v[84:99], v[68:71], v[100:103], 0
	v_mfma_f32_32x32x16_bf16 v[68:83], v[72:75], v[100:103], 0
	v_mfma_f32_32x32x16_bf16 v[84:99], v[224:227], v[104:107], v[84:99]
	v_mfma_f32_32x32x16_bf16 v[68:83], v[228:231], v[104:107], v[68:83]
	ds_read_b128 v[224:227], v66 offset:32768
	ds_read_b128 v[228:231], v66 offset:49152
	v_add3_u32 v66, s6, v204, v200
	s_waitcnt lgkmcnt(1)
	v_mfma_f32_32x32x16_bf16 v[84:99], v[224:227], v[108:111], v[84:99]
	s_waitcnt lgkmcnt(0)
	v_mfma_f32_32x32x16_bf16 v[68:83], v[228:231], v[108:111], v[68:83]
	ds_read_b128 v[224:227], v66 offset:32768
	ds_read_b128 v[228:231], v66 offset:49152
	v_add3_u32 v66, s6, v205, v200
	s_waitcnt lgkmcnt(1)
	v_mfma_f32_32x32x16_bf16 v[84:99], v[224:227], v[112:115], v[84:99]
	s_waitcnt lgkmcnt(0)
	v_mfma_f32_32x32x16_bf16 v[68:83], v[228:231], v[112:115], v[68:83]
	ds_read_b128 v[224:227], v66 offset:32768
	ds_read_b128 v[228:231], v66 offset:49152
	v_add3_u32 v66, s6, v206, v200
	s_waitcnt lgkmcnt(1)
	v_mfma_f32_32x32x16_bf16 v[84:99], v[224:227], v[116:119], v[84:99]
	s_waitcnt lgkmcnt(0)
	v_mfma_f32_32x32x16_bf16 v[68:83], v[228:231], v[116:119], v[68:83]
	ds_read_b128 v[224:227], v66 offset:32768
	ds_read_b128 v[228:231], v66 offset:49152
	v_add3_u32 v66, s6, v207, v200
	s_waitcnt lgkmcnt(1)
	v_mfma_f32_32x32x16_bf16 v[84:99], v[224:227], v[120:123], v[84:99]
	s_waitcnt lgkmcnt(0)
	v_mfma_f32_32x32x16_bf16 v[68:83], v[228:231], v[120:123], v[68:83]
	ds_read_b128 v[224:227], v66 offset:32768
	ds_read_b128 v[228:231], v66 offset:49152
	v_add3_u32 v66, s6, v208, v200
	s_waitcnt lgkmcnt(1)
	v_mfma_f32_32x32x16_bf16 v[84:99], v[224:227], v[124:127], v[84:99]
	s_waitcnt lgkmcnt(0)
	v_mfma_f32_32x32x16_bf16 v[68:83], v[228:231], v[124:127], v[68:83]
	ds_read_b128 v[224:227], v66 offset:32768
	ds_read_b128 v[228:231], v66 offset:49152
	v_add3_u32 v66, s6, v209, v200
	s_waitcnt lgkmcnt(1)
	v_mfma_f32_32x32x16_bf16 v[84:99], v[224:227], v[128:131], v[84:99]
	s_waitcnt lgkmcnt(0)
	v_mfma_f32_32x32x16_bf16 v[68:83], v[228:231], v[128:131], v[68:83]
	ds_read_b128 v[224:227], v66 offset:32768
	ds_read_b128 v[228:231], v66 offset:49152
	v_add3_u32 v66, s6, v211, v200
	s_waitcnt lgkmcnt(1)
	v_mfma_f32_32x32x16_bf16 v[84:99], v[224:227], v[132:135], v[84:99]
	s_waitcnt lgkmcnt(0)
	v_mfma_f32_32x32x16_bf16 v[68:83], v[228:231], v[132:135], v[68:83]
	ds_read_b128 v[224:227], v66 offset:32768
	ds_read_b128 v[228:231], v66 offset:49152
	v_add3_u32 v66, s6, v212, v200
	s_waitcnt lgkmcnt(1)
	v_mfma_f32_32x32x16_bf16 v[84:99], v[224:227], v[140:143], v[84:99]
	s_waitcnt lgkmcnt(0)
	v_mfma_f32_32x32x16_bf16 v[68:83], v[228:231], v[140:143], v[68:83]
	ds_read_b128 v[224:227], v66 offset:32768
	ds_read_b128 v[228:231], v66 offset:49152
	v_add3_u32 v66, s6, v213, v200
	s_waitcnt lgkmcnt(1)
	v_mfma_f32_32x32x16_bf16 v[84:99], v[224:227], v[136:139], v[84:99]
	s_waitcnt lgkmcnt(0)
	v_mfma_f32_32x32x16_bf16 v[68:83], v[228:231], v[136:139], v[68:83]
	ds_read_b128 v[224:227], v66 offset:32768
	ds_read_b128 v[228:231], v66 offset:49152
	s_waitcnt lgkmcnt(1)
	v_mfma_f32_32x32x16_bf16 v[84:99], v[224:227], v[144:147], v[84:99]
	s_waitcnt lgkmcnt(0)
	v_mfma_f32_32x32x16_bf16 v[68:83], v[228:231], v[144:147], v[68:83]
	s_setprio 0
	s_nop 8
	v_max_f32_e32 v66, v85, v85
	v_max_f32_e32 v219, v84, v84
	v_max_f32_e32 v66, v219, v66
	v_max3_f32 v66, v66, v86, v87
	v_max3_f32 v66, v66, v88, v89
	v_max3_f32 v66, v66, v90, v91
	v_max3_f32 v66, v66, v92, v93
	v_max3_f32 v66, v66, v94, v95
	v_max3_f32 v66, v66, v96, v97
	v_max3_f32 v66, v66, v98, v99
	v_max3_f32 v66, v66, v68, v69
	v_max3_f32 v66, v66, v70, v71
	v_max3_f32 v66, v66, v72, v73
	v_max3_f32 v66, v66, v74, v75
	v_max3_f32 v66, v66, v76, v77
	v_max3_f32 v66, v66, v78, v79
	v_max3_f32 v66, v66, v80, v81
	v_max3_f32 v66, v66, v82, v83
	v_mov_b32_e32 v219, v66
	s_nop 1
	v_permlane32_swap_b32_e32 v66, v219
	v_max_f32_e32 v219, v219, v219
	v_max_f32_e32 v66, v66, v66
	v_max_f32_e32 v66, v66, v219
	v_sub_f32_e32 v219, v66, v215
	v_cmp_ge_f32_e32 vcc, s34, v219
	s_cmp_eq_u64 vcc, exec
	s_cbranch_scc0 .Lresc_b
	v_mov_b32_e32 v219, 1.0
	s_branch .Lnor_b
.Lresc_b:
	v_max_f32_e32 v220, v215, v215
	v_sub_f32_e32 v219, v66, v215
	v_max_f32_e32 v66, v220, v66
	v_sub_f32_e32 v220, v215, v66
	v_mul_f32_e32 v220, 0x3dd53b94, v220
	v_exp_f32_e32 v220, v220
	v_cmp_ge_f32_e32 vcc, s34, v219
	s_cmp_eq_u64 vcc, exec
	s_cselect_b64 s[6:7], -1, 0
	v_cndmask_b32_e64 v219, v220, 1.0, s[6:7]
	v_cmp_gt_f32_e32 vcc, 1.0, v219
	s_cbranch_vccz .LBB0_1118
	s_and_saveexec_b64 s[26:27], s[4:5]
	ds_write_b32 v210, v219 offset:128
	s_or_b64 exec, exec, s[26:27]
	s_waitcnt lgkmcnt(0)
	v_add_u32_e32 v220, v185, v186
	ds_read_b128 v[224:227], v220 offset:224
	ds_read_b128 v[228:231], v220 offset:192
	ds_read_b128 v[232:235], v220 offset:160
	ds_read_b128 v[236:239], v220 offset:128
	s_waitcnt lgkmcnt(3)
	v_pk_mul_f32 v[62:63], v[62:63], v[224:225]
	s_waitcnt lgkmcnt(2)
	v_pk_mul_f32 v[58:59], v[58:59], v[228:229]
	s_waitcnt lgkmcnt(1)
	v_pk_mul_f32 v[54:55], v[54:55], v[232:233]
	v_pk_mul_f32 v[64:65], v[64:65], v[226:227]
	v_pk_mul_f32 v[60:61], v[60:61], v[230:231]
	v_pk_mul_f32 v[56:57], v[56:57], v[234:235]
	s_waitcnt lgkmcnt(0)
	v_pk_mul_f32 v[52:53], v[52:53], v[238:239]
	v_pk_mul_f32 v[50:51], v[50:51], v[236:237]
	v_pk_mul_f32 v[46:47], v[46:47], v[224:225]
	v_pk_mul_f32 v[42:43], v[42:43], v[228:229]
	v_pk_mul_f32 v[38:39], v[38:39], v[232:233]
	v_pk_mul_f32 v[48:49], v[48:49], v[226:227]
	v_pk_mul_f32 v[44:45], v[44:45], v[230:231]
	v_pk_mul_f32 v[40:41], v[40:41], v[234:235]
	v_pk_mul_f32 v[36:37], v[36:37], v[238:239]
	v_pk_mul_f32 v[34:35], v[34:35], v[236:237]
	v_pk_mul_f32 v[30:31], v[30:31], v[224:225]
	v_pk_mul_f32 v[26:27], v[26:27], v[228:229]
	v_pk_mul_f32 v[22:23], v[22:23], v[232:233]
	v_pk_mul_f32 v[32:33], v[32:33], v[226:227]
	v_pk_mul_f32 v[28:29], v[28:29], v[230:231]
	v_pk_mul_f32 v[24:25], v[24:25], v[234:235]
	v_pk_mul_f32 v[20:21], v[20:21], v[238:239]
	v_pk_mul_f32 v[18:19], v[18:19], v[236:237]
	v_pk_mul_f32 v[14:15], v[14:15], v[224:225]
	v_pk_mul_f32 v[10:11], v[10:11], v[228:229]
	v_pk_mul_f32 v[6:7], v[6:7], v[232:233]
	v_pk_mul_f32 v[16:17], v[16:17], v[226:227]
	v_pk_mul_f32 v[12:13], v[12:13], v[230:231]
	v_pk_mul_f32 v[8:9], v[8:9], v[234:235]
	v_pk_mul_f32 v[4:5], v[4:5], v[238:239]
	v_pk_mul_f32 v[2:3], v[2:3], v[236:237]

; #define SBAR() __builtin_amdgcn_sched_barrier(0)
; #define PV_WAIT(n) do { asm volatile("s_waitcnt lgkmcnt(" #n ")" ::: "memory"); SBAR(); } while (0)
; DEV void partialSM(f32x16& p0, f32x16& p1, float& m_reg, float& mn, float& alpha) {
;     ...
;   const float mnC = -mn * C;
; #pragma unroll
;   for (int r = 0; r < 16; ++r) p0[r] = fmaf(p0[r], C, mnC);
; #pragma unroll
;   for (int r = 0; r < 16; ++r) p1[r] = fmaf(p1[r], C, mnC);
; #pragma unroll
;   for (int r = 0; r < 16; ++r) p0[r] = __builtin_amdgcn_exp2f(p0[r]);
; }
; DEV void finishSM(f32x16& p0, f32x16& p1, float alpha, float& l_reg, bf16x8& pa0, bf16x8& pa1, bf16x8& pa2, bf16x8& pa3) {
; #pragma unroll
;   for (int r = 0; r < 16; ++r) p1[r] = __builtin_amdgcn_exp2f(p1[r]);
;   float ps = 0;
; #pragma unroll
;   for (int r = 0; r < 16; ++r) ps += p0[r];
; #pragma unroll
;   for (int r = 0; r < 16; ++r) ps += p1[r];
;   { auto rr = __builtin_amdgcn_permlane32_swap(__float_as_uint(ps), __float_as_uint(ps), false, false);
;     ps = __uint_as_float(rr[0]) + __uint_as_float(rr[1]); }
;   l_reg = l_reg * alpha + ps;
;     ...
;   PK4(p0, 0, pa0); PK4(p0, 8, pa1); PK4(p1, 0, pa2); PK4(p1, 8, pa3);
;     ...
; }
; DEV void pv_mma(f32x16& od, const VFrag& f, bf16x8 pa0, bf16x8 pa1, bf16x8 pa2, bf16x8 pa3) {
;     ...
;   __builtin_amdgcn_s_setprio(1);
;   od = __builtin_amdgcn_mfma_f32_32x32x16_bf16(pa0, PK(f.l0, f.h0), od, 0, 0, 0);
;   od = __builtin_amdgcn_mfma_f32_32x32x16_bf16(pa1, PK(f.l1, f.h1), od, 0, 0, 0);
;   od = __builtin_amdgcn_mfma_f32_32x32x16_bf16(pa2, PK(f.l2, f.h2), od, 0, 0, 0);
;   od = __builtin_amdgcn_mfma_f32_32x32x16_bf16(pa3, PK(f.l3, f.h3), od, 0, 0, 0);
;   __builtin_amdgcn_s_setprio(0);
;     ...
; }
; DEV void pv_d0(f32x16* o, int vb, bf16x8 pa0, bf16x8 pa1, bf16x8 pa2, bf16x8 pa3) {
;   VFrag fa, fb;
;   pv_read<0>(fa, vb);
;   pv_read<1>(fb, vb); PV_WAIT(8); pv_mma(o[0], fa, pa0, pa1, pa2, pa3); SBAR();
;   pv_read<2>(fa, vb); PV_WAIT(8); pv_mma(o[1], fb, pa0, pa1, pa2, pa3); SBAR();
;   pv_read<3>(fb, vb); PV_WAIT(8); pv_mma(o[2], fa, pa0, pa1, pa2, pa3); SBAR();
;   PV_WAIT(0); pv_mma(o[3], fb, pa0, pa1, pa2, pa3);
.Lnor_b:
	v_mul_f32_e32 v66, 0xbdd53b94, v215
	v_fmamk_f32 v84, v84, 0x3dd53b94, v66
	v_fmamk_f32 v85, v85, 0x3dd53b94, v66
	v_fmamk_f32 v86, v86, 0x3dd53b94, v66
	v_fmamk_f32 v87, v87, 0x3dd53b94, v66
	v_fmamk_f32 v88, v88, 0x3dd53b94, v66
	v_fmamk_f32 v89, v89, 0x3dd53b94, v66
	v_fmamk_f32 v90, v90, 0x3dd53b94, v66
	v_fmamk_f32 v91, v91, 0x3dd53b94, v66
	v_fmamk_f32 v92, v92, 0x3dd53b94, v66
	v_fmamk_f32 v93, v93, 0x3dd53b94, v66
	v_fmamk_f32 v94, v94, 0x3dd53b94, v66
	v_fmamk_f32 v95, v95, 0x3dd53b94, v66
	v_fmamk_f32 v96, v96, 0x3dd53b94, v66
	v_fmamk_f32 v97, v97, 0x3dd53b94, v66
	v_fmamk_f32 v98, v98, 0x3dd53b94, v66
	v_fmamk_f32 v99, v99, 0x3dd53b94, v66
	v_fmamk_f32 v68, v68, 0x3dd53b94, v66
	v_fmamk_f32 v69, v69, 0x3dd53b94, v66
	v_fmamk_f32 v70, v70, 0x3dd53b94, v66
	v_fmamk_f32 v71, v71, 0x3dd53b94, v66
	v_fmamk_f32 v72, v72, 0x3dd53b94, v66
	v_fmamk_f32 v73, v73, 0x3dd53b94, v66
	v_fmamk_f32 v74, v74, 0x3dd53b94, v66
	v_fmamk_f32 v75, v75, 0x3dd53b94, v66
	v_fmamk_f32 v76, v76, 0x3dd53b94, v66
	v_fmamk_f32 v77, v77, 0x3dd53b94, v66
	v_fmamk_f32 v78, v78, 0x3dd53b94, v66
	v_fmamk_f32 v79, v79, 0x3dd53b94, v66
	v_fmamk_f32 v80, v80, 0x3dd53b94, v66
	v_fmamk_f32 v81, v81, 0x3dd53b94, v66
	v_fmamk_f32 v82, v82, 0x3dd53b94, v66
	v_fmac_f32_e32 v66, 0x3dd53b94, v83
	v_exp_f32_e32 v83, v84
	v_exp_f32_e32 v84, v85
	v_exp_f32_e32 v85, v86
	v_exp_f32_e32 v86, v87
	v_exp_f32_e32 v87, v88
	v_exp_f32_e32 v88, v89
	v_exp_f32_e32 v89, v90
	v_exp_f32_e32 v90, v91
	v_exp_f32_e32 v91, v92
	v_exp_f32_e32 v92, v93
	v_exp_f32_e32 v93, v94
	v_exp_f32_e32 v94, v95
	v_exp_f32_e32 v95, v96
	v_exp_f32_e32 v96, v97
	v_exp_f32_e32 v97, v98
	v_exp_f32_e32 v98, v99
	v_exp_f32_e32 v99, v68
	v_add_f32_e32 v68, 0, v83
	v_add_f32_e32 v68, v84, v68
	v_add_f32_e32 v68, v85, v68
	v_add_f32_e32 v68, v86, v68
	v_add_f32_e32 v68, v87, v68
	v_add_f32_e32 v68, v88, v68
	v_add_f32_e32 v68, v89, v68
	v_add_f32_e32 v68, v90, v68
	v_add_f32_e32 v68, v91, v68
	v_add_f32_e32 v68, v92, v68
	v_add_f32_e32 v68, v93, v68
	v_add_f32_e32 v68, v94, v68
	v_add_f32_e32 v68, v95, v68
	v_exp_f32_e32 v220, v69
	v_add_f32_e32 v68, v96, v68
	v_exp_f32_e32 v221, v70
	v_add_f32_e32 v68, v97, v68
	v_exp_f32_e32 v222, v71
	v_add_f32_e32 v68, v98, v68
	v_exp_f32_e32 v224, v72
	v_add_f32_e32 v68, v99, v68
	v_exp_f32_e32 v225, v73
	v_add_f32_e32 v68, v220, v68
	v_exp_f32_e32 v226, v74
	v_add_f32_e32 v68, v221, v68
	v_exp_f32_e32 v227, v75
	v_add_f32_e32 v68, v222, v68
	v_exp_f32_e32 v228, v76
	v_add_f32_e32 v68, v224, v68
	v_exp_f32_e32 v229, v77
	v_add_f32_e32 v68, v225, v68
	v_exp_f32_e32 v230, v78
	v_add_f32_e32 v68, v226, v68
	v_exp_f32_e32 v231, v79
	v_add_f32_e32 v68, v227, v68
	v_exp_f32_e32 v232, v80
	v_add_f32_e32 v68, v228, v68
	v_exp_f32_e32 v233, v81
	v_add_f32_e32 v68, v229, v68
	v_exp_f32_e32 v234, v82
	v_add_f32_e32 v68, v230, v68
	v_exp_f32_e32 v66, v66
	v_add_f32_e32 v68, v231, v68
	v_add_f32_e32 v68, v232, v68
	v_add_f32_e32 v68, v233, v68
	v_add_f32_e32 v68, v234, v68
	v_add_f32_e32 v68, v66, v68
	v_mov_b32_e32 v69, v68
	s_nop 1
	v_permlane32_swap_b32_e32 v68, v69
	v_cvt_pk_bf16_f32 v70, v83, v84
	v_cvt_pk_bf16_f32 v71, v85, v86
	v_cvt_pk_bf16_f32 v72, v87, v88
	v_cvt_pk_bf16_f32 v73, v89, v90
	v_cvt_pk_bf16_f32 v74, v91, v92
	v_cvt_pk_bf16_f32 v75, v93, v94
	v_cvt_pk_bf16_f32 v76, v95, v96
	v_cvt_pk_bf16_f32 v77, v97, v98
	v_cvt_pk_bf16_f32 v78, v99, v220
	v_cvt_pk_bf16_f32 v79, v221, v222
	v_cvt_pk_bf16_f32 v80, v224, v225
	v_cvt_pk_bf16_f32 v81, v226, v227
	v_cvt_pk_bf16_f32 v82, v228, v229
	v_cvt_pk_bf16_f32 v83, v230, v231
	v_cvt_pk_bf16_f32 v84, v232, v233
	v_cvt_pk_bf16_f32 v85, v234, v66
	v_permlane32_swap_b32_e32 v70, v72
	v_permlane32_swap_b32_e32 v71, v73
	v_permlane32_swap_b32_e32 v74, v76
	v_permlane32_swap_b32_e32 v75, v77
	v_permlane32_swap_b32_e32 v78, v80
	v_permlane32_swap_b32_e32 v79, v81
	v_permlane32_swap_b32_e32 v82, v84
	v_permlane32_swap_b32_e32 v83, v85
	v_lshl_add_u32 v66, s37, 14, v214
	ds_read_b64_tr_b16 v[86:87], v66 offset:0
	ds_read_b64_tr_b16 v[88:89], v66 offset:0x800
	ds_read_b64_tr_b16 v[90:91], v66 offset:0x1000
	ds_read_b64_tr_b16 v[92:93], v66 offset:0x1800
	ds_read_b64_tr_b16 v[94:95], v66 offset:0x2000
	ds_read_b64_tr_b16 v[96:97], v66 offset:0x2800
	ds_read_b64_tr_b16 v[224:225], v66 offset:0x3000
	ds_read_b64_tr_b16 v[226:227], v66 offset:0x3800
	ds_read_b64_tr_b16 v[228:229], v66 offset:0x200
	ds_read_b64_tr_b16 v[230:231], v66 offset:0xa00
	ds_read_b64_tr_b16 v[232:233], v66 offset:0x1200
	ds_read_b64_tr_b16 v[234:235], v66 offset:0x1a00
	ds_read_b64_tr_b16 v[236:237], v66 offset:0x2200
	ds_read_b64_tr_b16 v[238:239], v66 offset:0x2a00
	ds_read_b64_tr_b16 v[240:241], v66 offset:0x3200
	ds_read_b64_tr_b16 v[242:243], v66 offset:0x3a00
	s_waitcnt lgkmcnt(8)
	s_setprio 1
	v_mfma_f32_32x32x16_bf16 v[50:65], v[70:73], v[86:89], v[50:65]
	v_mfma_f32_32x32x16_bf16 v[50:65], v[74:77], v[90:93], v[50:65]
	v_mfma_f32_32x32x16_bf16 v[50:65], v[78:81], v[94:97], v[50:65]
	v_mfma_f32_32x32x16_bf16 v[50:65], v[82:85], v[224:227], v[50:65]
	s_setprio 0
	ds_read_b64_tr_b16 v[86:87], v66 offset:0x400
	ds_read_b64_tr_b16 v[88:89], v66 offset:0xc00
	ds_read_b64_tr_b16 v[90:91], v66 offset:0x1400
	ds_read_b64_tr_b16 v[92:93], v66 offset:0x1c00
	ds_read_b64_tr_b16 v[94:95], v66 offset:0x2400
	ds_read_b64_tr_b16 v[96:97], v66 offset:0x2c00
	ds_read_b64_tr_b16 v[224:225], v66 offset:0x3400
	ds_read_b64_tr_b16 v[226:227], v66 offset:0x3c00
	s_waitcnt lgkmcnt(8)
	s_setprio 1
	v_mfma_f32_32x32x16_bf16 v[34:49], v[70:73], v[228:231], v[34:49]
	v_mfma_f32_32x32x16_bf16 v[34:49], v[74:77], v[232:235], v[34:49]
	v_mfma_f32_32x32x16_bf16 v[34:49], v[78:81], v[236:239], v[34:49]
	v_mfma_f32_32x32x16_bf16 v[34:49], v[82:85], v[240:243], v[34:49]
	s_setprio 0
	ds_read_b64_tr_b16 v[228:229], v66 offset:0x600
	ds_read_b64_tr_b16 v[230:231], v66 offset:0xe00
	ds_read_b64_tr_b16 v[232:233], v66 offset:0x1600
	ds_read_b64_tr_b16 v[234:235], v66 offset:0x1e00
	ds_read_b64_tr_b16 v[236:237], v66 offset:0x2600
	ds_read_b64_tr_b16 v[238:239], v66 offset:0x2e00
	ds_read_b64_tr_b16 v[240:241], v66 offset:0x3600
	ds_read_b64_tr_b16 v[242:243], v66 offset:0x3e00
	s_waitcnt lgkmcnt(8)
	s_setprio 1
	v_mfma_f32_32x32x16_bf16 v[18:33], v[70:73], v[86:89], v[18:33]
	v_mfma_f32_32x32x16_bf16 v[18:33], v[74:77], v[90:93], v[18:33]
	v_mfma_f32_32x32x16_bf16 v[18:33], v[78:81], v[94:97], v[18:33]
	v_mfma_f32_32x32x16_bf16 v[18:33], v[82:85], v[224:227], v[18:33]
	s_setprio 0
	s_waitcnt lgkmcnt(0)
	s_setprio 1
	v_mfma_f32_32x32x16_bf16 v[2:17], v[70:73], v[228:231], v[2:17]
	v_mfma_f32_32x32x16_bf16 v[2:17], v[74:77], v[232:235], v[2:17]
	v_mfma_f32_32x32x16_bf16 v[2:17], v[78:81], v[236:239], v[2:17]
	v_mfma_f32_32x32x16_bf16 v[2:17], v[82:85], v[240:243], v[2:17]
	s_setprio 0
	s_cmp_gt_u32 s38, 61
	s_cbranch_scc1 .LBB0_1126
; DEV int ltid() { int t = threadIdx.x; asm volatile("" : "+v"(t)); return t; }
; DEV unsigned cvt_pk4_fp8(f32x4 v) { unsigned r = 0; r = __builtin_amdgcn_cvt_pk_fp8_f32(v[0], v[1], r, false); r = __builtin_amdgcn_cvt_pk_fp8_f32(v[2], v[3], r, true); return r; }
; DEV void fill_load(CParams& p, int wg, int slot, f32x4 (&ld)[4]) {
;   const FillDesc d = fill_decode(p, wg, slot); const int tid = ltid(), tx = tid & 15, ty = tid >> 4;
;   const float* sp = d.src + (long)(d.kh + 4 * ty) * d.ldsrc + d.n0 + 4 * tx;
; #pragma unroll
;   for (int r = 0; r < 4; ++r) ld[r] = *(const f32x4*)(sp + (long)r * d.ldsrc);
; }
; DEV void fill_write(const f32x4 (&ld)[4], int bufsel) {
;   extern __shared__ __attribute__((aligned(16))) char shm[];
;   unsigned* T = (unsigned*)(shm + FILL_LDS_OFF + bufsel * FILL_TB); const int tid = ltid(), tx = tid & 15, ty = tid >> 4;
;   constexpr float WS = (float)(1 << FP8_WSCALE_LOG2_);
; #pragma unroll
;   for (int j = 0; j < 4; ++j) T[(4 * tx + j) * 33 + ty] = cvt_pk4_fp8((f32x4){ld[0][j] * WS, ld[1][j] * WS, ld[2][j] * WS, ld[3][j] * WS});
; }
; DEV void attn_unit(const bf16_t* __restrict__ Qb, const bf16_t* __restrict__ Kh, const bf16_t* __restrict__ Vh, const float* __restrict__ rp, bf16_t* __restrict__ Ob, CParams& fp, int fwg, int fbase, int fn) {
;     ...
;     if (j < fn) { fill_write(fld, j & 1); if (j + 1 < fn) fill_load(fp, fwg, fbase + j + 1, fld); }
	s_waitcnt vmcnt(3)
	v_mul_f32_e32 v71, 0x42800000, v168
	s_waitcnt vmcnt(2)
	v_mul_f32_e32 v72, 0x42800000, v172
	v_cvt_pk_fp8_f32 v73, v71, v72
	s_waitcnt vmcnt(1)
	v_mul_f32_e32 v71, 0x42800000, v176
	s_waitcnt vmcnt(0)
	v_mul_f32_e32 v72, 0x42800000, v180
	v_cvt_pk_fp8_f32 v73, v71, v72 op_sel:[0,0,1]
	v_mul_f32_e32 v71, 0x42800000, v169
	v_mul_f32_e32 v72, 0x42800000, v173
	v_cvt_pk_fp8_f32 v74, v71, v72
	v_mul_f32_e32 v71, 0x42800000, v177
	v_mul_f32_e32 v72, 0x42800000, v181
	v_cvt_pk_fp8_f32 v74, v71, v72 op_sel:[0,0,1]
	v_mul_f32_e32 v71, 0x42800000, v170
	v_mul_f32_e32 v72, 0x42800000, v174
	v_cvt_pk_fp8_f32 v77, v71, v72
	v_mul_f32_e32 v71, 0x42800000, v171
	v_mul_f32_e32 v72, 0x42800000, v175
	v_cvt_pk_fp8_f32 v78, v71, v72
	v_mul_f32_e32 v75, 0x42800000, v178
	v_mul_f32_e32 v76, 0x42800000, v182
	v_mul_f32_e32 v71, 0x42800000, v179
	v_mul_f32_e32 v72, 0x42800000, v183
	v_cvt_pk_fp8_f32 v77, v75, v76 op_sel:[0,0,1]
	v_cvt_pk_fp8_f32 v78, v71, v72 op_sel:[0,0,1]
	s_mul_i32 s56, s37, 0x2200
	s_cmp_eq_u32 s35, 59
	v_add_u32_e32 v66, s56, v245
	ds_write2_b32 v66, v73, v74 offset1:33
	ds_write2_b32 v66, v77, v78 offset0:66 offset1:99
	s_cbranch_scc1 .LBB0_1126
	global_load_dwordx4 v[168:171], v248, s[62:63]
	global_load_dwordx4 v[172:175], v249, s[62:63]
	global_load_dwordx4 v[176:179], v250, s[62:63]
	global_load_dwordx4 v[180:183], v251, s[62:63]
	s_add_u32 s62, s62, 0x800000
	s_addc_u32 s63, s63, 0
